# combo12 + gate-up K-loop: hipcc's s_waitcnt vmcnt(0) at the top of every iteration (drained the LDS-DMA lookahead) removed from the loop body; the peeled first iteration keeps it
# speedup vs baseline: 1.0053x; 1.0053x over previous
.LBB0_1035:
	ds_read_b128 v[136:139], v150
	ds_read_b128 v[156:159], v150 offset:2048
	ds_read_b128 v[140:143], v151
	ds_read_b128 v[160:163], v151 offset:2048
	ds_read_b128 v[164:167], v150 offset:16384
	ds_read_b128 v[172:175], v150 offset:18432
	ds_read_b128 v[168:171], v151 offset:16384
	ds_read_b128 v[176:179], v151 offset:18432
	s_add_u32 s28, s24, 0x80
	s_addc_u32 s29, s25, 0
	s_cmp_eq_u32 s77, 4
	s_cselect_b32 s29, s11, s29
	s_cselect_b32 s28, s10, s28
	s_cselect_b32 s80, s27, s75
	s_cselect_b32 s37, s23, s76
	s_cselect_b32 s36, s22, s19
	ds_read_b128 v[194:197], v148
	ds_read_b128 v[228:231], v148 offset:2048
	ds_read_b128 v[198:201], v149
	ds_read_b128 v[232:235], v149 offset:2048
	ds_read_b128 v[236:239], v148 offset:4096
	ds_read_b128 v[244:247], v148 offset:6144
	ds_read_b128 v[240:243], v149 offset:4096
	ds_read_b128 v[248:251], v149 offset:6144
	v_mbcnt_lo_u32_b32 v40, -1, 0
	v_mbcnt_hi_u32_b32 v40, -1, v40
	s_mov_b32 s78, s61
	v_lshlrev_b32_e32 v40, 3, v40
	s_add_i32 m0, s35, 0xc000
	v_lshl_or_b32 v40, s78, 9, v40
	v_add_u32_e32 v40, s74, v40
	ds_read_b32 v40, v40 offset:4
	s_waitcnt lgkmcnt(0)
	v_lshlrev_b32_e32 v41, 10, v40
	v_and_or_b32 v41, v41, s69, v154
	v_bfe_u32 v40, v40, 16, 16
	v_lshl_or_b32 v40, v40, 10, v154
	global_load_lds_dwordx4 v41, s[24:25]
	s_add_i32 m0, s35, 0xe000
	s_nop 0
	global_load_lds_dwordx4 v40, s[24:25]
	s_waitcnt vmcnt(8)
	s_waitcnt lgkmcnt(0)
	s_barrier
	s_setprio 1
	v_mfma_f32_16x16x128_f8f6f4 v[132:135], v[136:143], v[194:201], v[132:135]
	v_mfma_f32_16x16x128_f8f6f4 v[124:127], v[156:163], v[194:201], v[124:127]
	v_mfma_f32_16x16x128_f8f6f4 v[116:119], v[136:143], v[228:235], v[116:119]
	v_mfma_f32_16x16x128_f8f6f4 v[108:111], v[156:163], v[228:235], v[108:111]
	v_mfma_f32_16x16x128_f8f6f4 v[144:147], v[136:143], v[236:243], v[100:103]
	v_mfma_f32_16x16x128_f8f6f4 v[180:183], v[156:163], v[236:243], v[92:95]
	v_mfma_f32_16x16x128_f8f6f4 v[186:189], v[136:143], v[244:251], v[84:87]
	v_mfma_f32_16x16x128_f8f6f4 v[190:193], v[156:163], v[244:251], v[76:79]
	s_setprio 0
	s_setprio 1
	v_mfma_f32_16x16x128_f8f6f4 v[128:131], v[164:171], v[194:201], v[128:131]
	v_mfma_f32_16x16x128_f8f6f4 v[120:123], v[172:179], v[194:201], v[120:123]
	v_mfma_f32_16x16x128_f8f6f4 v[112:115], v[164:171], v[228:235], v[112:115]
	v_mfma_f32_16x16x128_f8f6f4 v[104:107], v[172:179], v[228:235], v[104:107]
	v_mfma_f32_16x16x128_f8f6f4 v[202:205], v[164:171], v[236:243], v[96:99]
	v_mfma_f32_16x16x128_f8f6f4 v[206:209], v[172:179], v[236:243], v[88:91]
	v_mfma_f32_16x16x128_f8f6f4 v[210:213], v[164:171], v[244:251], v[80:83]
	v_mfma_f32_16x16x128_f8f6f4 v[214:217], v[172:179], v[244:251], v[72:75]
	s_setprio 0
	s_barrier
	v_mov_b32_e32 v40, v152
	s_mov_b32 m0, s44
	s_nop 2
	ds_read_b128 v[72:75], v148 offset:16384
	ds_read_b128 v[80:83], v148 offset:18432
	ds_read_b128 v[76:79], v149 offset:16384
	ds_read_b128 v[84:87], v149 offset:18432
	ds_read_b128 v[88:91], v148 offset:20480
	ds_read_b128 v[96:99], v148 offset:22528
	ds_read_b128 v[92:95], v149 offset:20480
	ds_read_b128 v[100:103], v149 offset:22528
	s_add_u32 s78, s36, 0x20000
	global_load_lds_dwordx4 v40, s[36:37]
	v_mov_b32_e32 v40, v153
	s_mov_b32 m0, s49
	s_addc_u32 s79, s37, 0
	global_load_lds_dwordx4 v40, s[36:37]
	v_mov_b32_e32 v40, v152
	s_mov_b32 m0, s50
	s_nop 0
	global_load_lds_dwordx4 v40, s[78:79]
	v_mov_b32_e32 v40, v153
	s_mov_b32 m0, s51
	s_nop 0
	global_load_lds_dwordx4 v40, s[78:79]
	v_mbcnt_lo_u32_b32 v40, -1, 0
	v_mbcnt_hi_u32_b32 v40, -1, v40
	s_mov_b32 s78, s61
	v_lshlrev_b32_e32 v40, 3, v40
	v_lshl_or_b32 v40, s78, 9, v40
	s_lshl_b32 s78, s80, 12
	s_add_i32 s78, s78, 0
	s_add_i32 s78, s78, 0x21000
	v_add_u32_e32 v40, s78, v40
	ds_read_b32 v40, v40
	s_mov_b32 m0, s35
	s_waitcnt lgkmcnt(0)
	v_lshlrev_b32_e32 v41, 10, v40
	v_and_or_b32 v41, v41, s69, v154
	v_bfe_u32 v40, v40, 16, 16
	v_lshl_or_b32 v40, v40, 10, v154
	global_load_lds_dwordx4 v41, s[28:29]
	s_mov_b32 m0, s54
	s_nop 0
	global_load_lds_dwordx4 v40, s[28:29]
	s_waitcnt vmcnt(8)
	s_waitcnt lgkmcnt(0)
	s_barrier
	s_setprio 1
	v_mfma_f32_16x16x128_f8f6f4 v[48:51], v[136:143], v[80:87], v[48:51]
	v_mfma_f32_16x16x128_f8f6f4 v[36:39], v[156:163], v[80:87], v[36:39]
	v_mfma_f32_16x16x128_f8f6f4 v[28:31], v[136:143], v[88:95], v[28:31]
	v_mfma_f32_16x16x128_f8f6f4 v[20:23], v[156:163], v[88:95], v[20:23]
	v_mfma_f32_16x16x128_f8f6f4 v[12:15], v[136:143], v[96:103], v[12:15]
	v_mfma_f32_16x16x128_f8f6f4 v[4:7], v[156:163], v[96:103], v[4:7]
	v_mfma_f32_16x16x128_f8f6f4 v[40:43], v[136:143], v[72:79], v[68:71]
	v_mfma_f32_16x16x128_f8f6f4 v[52:55], v[156:163], v[72:79], v[60:63]
	s_setprio 0
	s_setprio 1
	v_mfma_f32_16x16x128_f8f6f4 v[64:67], v[164:171], v[72:79], v[64:67]
	v_mfma_f32_16x16x128_f8f6f4 v[56:59], v[172:179], v[72:79], v[56:59]
	v_mfma_f32_16x16x128_f8f6f4 v[44:47], v[164:171], v[80:87], v[44:47]
	v_mfma_f32_16x16x128_f8f6f4 v[32:35], v[172:179], v[80:87], v[32:35]
	v_mfma_f32_16x16x128_f8f6f4 v[24:27], v[164:171], v[88:95], v[24:27]
	v_mfma_f32_16x16x128_f8f6f4 v[16:19], v[172:179], v[88:95], v[16:19]
	v_mfma_f32_16x16x128_f8f6f4 v[8:11], v[164:171], v[96:103], v[8:11]
	v_mfma_f32_16x16x128_f8f6f4 v[0:3], v[172:179], v[96:103], v[0:3]
	s_setprio 0
	s_barrier
	ds_read_b128 v[136:139], v150 offset:32768
	ds_read_b128 v[156:159], v150 offset:34816
	ds_read_b128 v[140:143], v151 offset:32768
	ds_read_b128 v[160:163], v151 offset:34816
	ds_read_b128 v[164:167], v150 offset:49152
	ds_read_b128 v[172:175], v150 offset:51200
	ds_read_b128 v[168:171], v151 offset:49152
	ds_read_b128 v[176:179], v151 offset:51200
	ds_read_b128 v[68:71], v148 offset:32768
	ds_read_b128 v[194:197], v148 offset:34816
	ds_read_b128 v[72:75], v149 offset:32768
	ds_read_b128 v[198:201], v149 offset:34816
	ds_read_b128 v[228:231], v148 offset:36864
	ds_read_b128 v[236:239], v148 offset:38912
	ds_read_b128 v[232:235], v149 offset:36864
	ds_read_b128 v[240:243], v149 offset:38912
	v_mbcnt_lo_u32_b32 v60, -1, 0
	v_mbcnt_hi_u32_b32 v60, -1, v60
	s_mov_b32 s79, s61
	v_lshlrev_b32_e32 v60, 3, v60
	s_mov_b32 m0, s55
	v_lshl_or_b32 v60, s79, 9, v60
	v_add_u32_e32 v60, s78, v60
	ds_read_b32 v60, v60 offset:4
	s_waitcnt lgkmcnt(0)
	v_lshlrev_b32_e32 v61, 10, v60
	v_and_or_b32 v61, v61, s69, v154
	v_bfe_u32 v60, v60, 16, 16
	v_lshl_or_b32 v60, v60, 10, v154
	global_load_lds_dwordx4 v61, s[28:29]
	s_mov_b32 m0, s56
	s_nop 0
	global_load_lds_dwordx4 v60, s[28:29]
	s_waitcnt vmcnt(8)
	s_waitcnt lgkmcnt(0)
	s_barrier
	s_setprio 1
	v_mfma_f32_16x16x128_f8f6f4 v[132:135], v[136:143], v[68:75], v[132:135]
	v_mfma_f32_16x16x128_f8f6f4 v[124:127], v[156:163], v[68:75], v[124:127]
	v_mfma_f32_16x16x128_f8f6f4 v[116:119], v[136:143], v[194:201], v[116:119]
	v_mfma_f32_16x16x128_f8f6f4 v[108:111], v[156:163], v[194:201], v[108:111]
	v_mfma_f32_16x16x128_f8f6f4 v[100:103], v[136:143], v[228:235], v[144:147]
	v_mfma_f32_16x16x128_f8f6f4 v[92:95], v[156:163], v[228:235], v[180:183]
	v_mfma_f32_16x16x128_f8f6f4 v[84:87], v[136:143], v[236:243], v[186:189]
	v_mfma_f32_16x16x128_f8f6f4 v[76:79], v[156:163], v[236:243], v[190:193]
	s_setprio 0
	s_setprio 1
	v_mfma_f32_16x16x128_f8f6f4 v[128:131], v[164:171], v[68:75], v[128:131]
	v_mfma_f32_16x16x128_f8f6f4 v[120:123], v[172:179], v[68:75], v[120:123]
	v_mfma_f32_16x16x128_f8f6f4 v[112:115], v[164:171], v[194:201], v[112:115]
	v_mfma_f32_16x16x128_f8f6f4 v[104:107], v[172:179], v[194:201], v[104:107]
	v_mfma_f32_16x16x128_f8f6f4 v[96:99], v[164:171], v[228:235], v[202:205]
	v_mfma_f32_16x16x128_f8f6f4 v[88:91], v[172:179], v[228:235], v[206:209]
	v_mfma_f32_16x16x128_f8f6f4 v[80:83], v[164:171], v[236:243], v[210:213]
	v_mfma_f32_16x16x128_f8f6f4 v[72:75], v[172:179], v[236:243], v[214:217]
	s_setprio 0
	s_barrier
	v_mov_b32_e32 v184, v152
	ds_read_b128 v[194:197], v148 offset:49152
	ds_read_b128 v[228:231], v148 offset:51200
	ds_read_b128 v[198:201], v149 offset:49152
	ds_read_b128 v[232:235], v149 offset:51200
	ds_read_b128 v[236:239], v148 offset:53248
	ds_read_b128 v[244:247], v148 offset:55296
	ds_read_b128 v[240:243], v149 offset:53248
	ds_read_b128 v[248:251], v149 offset:55296
	s_mov_b32 m0, s57
	v_lshl_add_u64 v[60:61], s[36:37], 0, v[184:185]
	v_lshl_add_u64 v[60:61], v[60:61], 0, s[46:47]
	v_mov_b32_e32 v184, v153
	global_load_lds_dwordx4 v[60:61], off
	s_mov_b32 m0, s59
	v_lshl_add_u64 v[60:61], s[36:37], 0, v[184:185]
	v_lshl_add_u64 v[60:61], v[60:61], 0, s[46:47]
	global_load_lds_dwordx4 v[60:61], off
	s_add_u32 s36, s36, 0x20080
	v_mov_b32_e32 v60, v152
	s_addc_u32 s37, s37, 0
	s_mov_b32 m0, s66
	s_nop 0
	global_load_lds_dwordx4 v60, s[36:37]
	v_mov_b32_e32 v60, v153
	s_mov_b32 m0, s67
	s_nop 0
	global_load_lds_dwordx4 v60, s[36:37]
	v_mbcnt_lo_u32_b32 v60, -1, 0
	v_mbcnt_hi_u32_b32 v60, -1, v60
	s_mov_b32 s36, s61
	v_lshlrev_b32_e32 v60, 3, v60
	s_mov_b32 m0, s64
	v_lshl_or_b32 v60, s36, 9, v60
	v_add_u32_e32 v60, s78, v60
	ds_read_b32 v62, v60
	s_waitcnt lgkmcnt(0)
	v_lshlrev_b32_e32 v60, 10, v62
	v_and_or_b32 v184, v60, s69, v154
	s_nop 0
	v_lshl_add_u64 v[60:61], s[28:29], 0, v[184:185]
	v_lshl_add_u64 v[60:61], v[60:61], 0, s[46:47]
	global_load_lds_dwordx4 v[60:61], off
	v_bfe_u32 v60, v62, 16, 16
	v_lshl_or_b32 v184, v60, 10, v154
	s_mov_b32 m0, s65
	v_lshl_add_u64 v[60:61], s[28:29], 0, v[184:185]
	v_lshl_add_u64 v[60:61], v[60:61], 0, s[46:47]
	global_load_lds_dwordx4 v[60:61], off
	s_waitcnt vmcnt(8)
	s_waitcnt lgkmcnt(0)
	s_barrier
	s_setprio 1
	v_mfma_f32_16x16x128_f8f6f4 v[68:71], v[136:143], v[194:201], v[40:43]
	v_mfma_f32_16x16x128_f8f6f4 v[60:63], v[156:163], v[194:201], v[52:55]
	v_mfma_f32_16x16x128_f8f6f4 v[48:51], v[136:143], v[228:235], v[48:51]
	v_mfma_f32_16x16x128_f8f6f4 v[36:39], v[156:163], v[228:235], v[36:39]
	v_mfma_f32_16x16x128_f8f6f4 v[28:31], v[136:143], v[236:243], v[28:31]
	v_mfma_f32_16x16x128_f8f6f4 v[20:23], v[156:163], v[236:243], v[20:23]
	v_mfma_f32_16x16x128_f8f6f4 v[12:15], v[136:143], v[244:251], v[12:15]
	v_mfma_f32_16x16x128_f8f6f4 v[4:7], v[156:163], v[244:251], v[4:7]
	s_setprio 0
	s_setprio 1
	v_mfma_f32_16x16x128_f8f6f4 v[64:67], v[164:171], v[194:201], v[64:67]
	v_mfma_f32_16x16x128_f8f6f4 v[56:59], v[172:179], v[194:201], v[56:59]
	v_mfma_f32_16x16x128_f8f6f4 v[44:47], v[164:171], v[228:235], v[44:47]
	v_mfma_f32_16x16x128_f8f6f4 v[32:35], v[172:179], v[228:235], v[32:35]
	v_mfma_f32_16x16x128_f8f6f4 v[24:27], v[164:171], v[236:243], v[24:27]
	v_mfma_f32_16x16x128_f8f6f4 v[16:19], v[172:179], v[236:243], v[16:19]
	v_mfma_f32_16x16x128_f8f6f4 v[8:11], v[164:171], v[244:251], v[8:11]
	v_mfma_f32_16x16x128_f8f6f4 v[0:3], v[172:179], v[244:251], v[0:3]
	s_setprio 0
	s_barrier
	s_add_i32 s77, s77, 2
	s_add_u32 s24, s24, 0x100
	s_addc_u32 s25, s25, 0
	s_add_u32 s19, s19, 0x100
	s_addc_u32 s76, s76, 0
	s_cmp_gt_u32 s77, 5
	s_cbranch_scc0 .LBB0_1035
	s_and_b64 vcc, exec, s[8:9]
	s_mov_b32 s36, s26
	s_mov_b32 s28, s73
	s_mov_b64 s[8:9], 0
	s_cbranch_vccz .LBB0_1039
	s_add_i32 s8, s72, 2
	s_mul_i32 s9, s8, s31
	s_mul_hi_u32 s19, s8, s0
	s_add_i32 s19, s19, s9
	s_mul_i32 s8, s8, s0
	s_add_u32 s24, s8, s1
	s_addc_u32 s25, s19, s40
	v_mov_b64_e32 v[40:41], s[4:5]
	v_cmp_ge_i64_e32 vcc, s[24:25], v[40:41]
	s_mov_b64 s[8:9], 0
	s_mov_b32 s28, s73
	s_mov_b32 s36, s26
	s_cbranch_vccnz .LBB0_1039
	s_ashr_i32 s8, s24, 31
	s_lshr_b32 s8, s8, 29
	s_add_i32 s8, s24, s8
	s_ashr_i32 s9, s8, 3
	s_and_b32 s8, s8, -8
	s_sub_i32 s8, s24, s8
	s_lshr_b32 s19, s8, 31
	s_add_i32 s19, s33, s19
	s_mul_i32 s8, s19, s8
	s_add_i32 s8, s8, s9
	s_ashr_i32 s9, s8, 31
	s_lshr_b32 s9, s9, 26
	s_add_i32 s9, s8, s9
	s_ashr_i32 s19, s9, 6
	s_lshl_b32 s19, s19, 3
	s_sub_i32 s24, s33, s19
	s_min_i32 s24, s24, 8
	s_abs_i32 s25, s24
	v_cvt_f32_u32_e32 v40, s25
	s_sub_i32 s29, 0, s25
	s_andn2_b32 s9, s9, 63
	s_sub_i32 s8, s8, s9
	v_rcp_iflag_f32_e32 v40, v40
	s_abs_i32 s9, s8
	s_xor_b32 s28, s8, s24
	s_ashr_i32 s28, s28, 31
	v_mul_f32_e32 v40, 0x4f7ffffe, v40
	v_cvt_u32_f32_e32 v40, v40
	s_nop 0
	v_readfirstlane_b32 s36, v40
	s_mul_i32 s29, s29, s36
	s_mul_hi_u32 s29, s36, s29
	s_add_i32 s36, s36, s29
	s_mul_hi_u32 s29, s9, s36
	s_mul_i32 s36, s29, s25
	s_sub_i32 s9, s9, s36
	s_add_i32 s37, s29, 1
	s_sub_i32 s36, s9, s25
	s_cmp_ge_u32 s9, s25
	s_cselect_b32 s29, s37, s29
	s_cselect_b32 s9, s36, s9
	s_add_i32 s36, s29, 1
	s_cmp_ge_u32 s9, s25
	s_cselect_b32 s9, s36, s29
	s_xor_b32 s9, s9, s28
	s_sub_i32 s36, s9, s28
	s_mul_i32 s9, s36, s24
	s_sub_i32 s8, s8, s9
	s_add_i32 s28, s8, s19
	s_mov_b64 s[8:9], -1
